# clamp-relu topic loop with bank-aware split accumulators (134 VALU per topic)
# baseline (speedup 1.0000x reference)
.Ltopic_loop:
	v_add_u32_e32 v152, s0, v86
	ds_read_b128 v[136:139], v152
	ds_read_b128 v[140:143], v152 offset:32
	ds_read_b128 v[144:147], v152 offset:64
	ds_read_b128 v[148:151], v152 offset:96
	s_addk_i32 s0, 0x200
	s_waitcnt lgkmcnt(4)
	v_add_f32_e64 v104, v2, v88 clamp
	v_add_f32_e64 v108, v6, v88 clamp
	v_add_f32_e64 v112, v10, v88 clamp
	v_add_f32_e64 v116, v14, v88 clamp
	v_add_f32_e64 v105, v3, v89 clamp
	v_add_f32_e64 v109, v7, v89 clamp
	v_add_f32_e64 v113, v11, v89 clamp
	v_add_f32_e64 v117, v15, v89 clamp
	v_add_f32_e64 v106, v4, v90 clamp
	v_add_f32_e64 v110, v8, v90 clamp
	v_add_f32_e64 v114, v12, v90 clamp
	v_add_f32_e64 v118, v16, v90 clamp
	v_add_f32_e64 v107, v5, v91 clamp
	v_add_f32_e64 v111, v9, v91 clamp
	v_add_f32_e64 v115, v13, v91 clamp
	v_add_f32_e64 v119, v17, v91 clamp
	v_mul_f32_e32 v153, v66, v104
	v_mul_f32_e32 v155, v66, v108
	v_mul_f32_e32 v157, v66, v112
	v_mul_f32_e32 v159, v66, v116
	v_mul_f32_e32 v154, v67, v105
	v_mul_f32_e32 v156, v67, v109
	v_mul_f32_e32 v158, v67, v113
	v_mul_f32_e32 v164, v67, v117
	v_fmac_f32_e32 v153, v68, v106
	v_fmac_f32_e32 v155, v68, v110
	v_fmac_f32_e32 v157, v68, v114
	v_fmac_f32_e32 v159, v68, v118
	v_fmac_f32_e32 v154, v69, v107
	v_fmac_f32_e32 v156, v69, v111
	v_fmac_f32_e32 v158, v69, v115
	v_fmac_f32_e32 v164, v69, v119
	v_add_f32_e64 v120, v18, v92 clamp
	v_add_f32_e64 v124, v22, v92 clamp
	v_add_f32_e64 v128, v26, v92 clamp
	v_add_f32_e64 v132, v30, v92 clamp
	v_add_f32_e64 v121, v19, v93 clamp
	v_add_f32_e64 v125, v23, v93 clamp
	v_add_f32_e64 v129, v27, v93 clamp
	v_add_f32_e64 v133, v31, v93 clamp
	v_add_f32_e64 v122, v20, v94 clamp
	v_add_f32_e64 v126, v24, v94 clamp
	v_add_f32_e64 v130, v28, v94 clamp
	v_add_f32_e64 v134, v32, v94 clamp
	v_add_f32_e64 v123, v21, v95 clamp
	v_add_f32_e64 v127, v25, v95 clamp
	v_add_f32_e64 v131, v29, v95 clamp
	v_add_f32_e64 v135, v33, v95 clamp
	v_fmac_f32_e32 v153, v70, v120
	v_fmac_f32_e32 v155, v70, v124
	v_fmac_f32_e32 v157, v70, v128
	v_fmac_f32_e32 v159, v70, v132
	v_fmac_f32_e32 v154, v71, v121
	v_fmac_f32_e32 v156, v71, v125
	v_fmac_f32_e32 v158, v71, v129
	v_fmac_f32_e32 v164, v71, v133
	v_fmac_f32_e32 v153, v72, v122
	v_fmac_f32_e32 v155, v72, v126
	v_fmac_f32_e32 v157, v72, v130
	v_fmac_f32_e32 v159, v72, v134
	v_fmac_f32_e32 v154, v73, v123
	v_fmac_f32_e32 v156, v73, v127
	v_fmac_f32_e32 v158, v73, v131
	v_fmac_f32_e32 v164, v73, v135
	v_add_f32_e64 v104, v34, v96 clamp
	v_add_f32_e64 v108, v38, v96 clamp
	v_add_f32_e64 v112, v42, v96 clamp
	v_add_f32_e64 v116, v46, v96 clamp
	v_add_f32_e64 v105, v35, v97 clamp
	v_add_f32_e64 v109, v39, v97 clamp
	v_add_f32_e64 v113, v43, v97 clamp
	v_add_f32_e64 v117, v47, v97 clamp
	v_add_f32_e64 v106, v36, v98 clamp
	v_add_f32_e64 v110, v40, v98 clamp
	v_add_f32_e64 v114, v44, v98 clamp
	v_add_f32_e64 v118, v48, v98 clamp
	v_add_f32_e64 v107, v37, v99 clamp
	v_add_f32_e64 v111, v41, v99 clamp
	v_add_f32_e64 v115, v45, v99 clamp
	v_add_f32_e64 v119, v49, v99 clamp
	v_fmac_f32_e32 v153, v74, v104
	v_fmac_f32_e32 v155, v74, v108
	v_fmac_f32_e32 v157, v74, v112
	v_fmac_f32_e32 v159, v74, v116
	v_fmac_f32_e32 v154, v75, v105
	v_fmac_f32_e32 v156, v75, v109
	v_fmac_f32_e32 v158, v75, v113
	v_fmac_f32_e32 v164, v75, v117
	v_fmac_f32_e32 v153, v76, v106
	v_fmac_f32_e32 v155, v76, v110
	v_fmac_f32_e32 v157, v76, v114
	v_fmac_f32_e32 v159, v76, v118
	v_fmac_f32_e32 v154, v77, v107
	v_fmac_f32_e32 v156, v77, v111
	v_fmac_f32_e32 v158, v77, v115
	v_fmac_f32_e32 v164, v77, v119
	v_add_f32_e64 v120, v50, v100 clamp
	v_add_f32_e64 v124, v54, v100 clamp
	v_add_f32_e64 v128, v58, v100 clamp
	v_add_f32_e64 v132, v62, v100 clamp
	v_add_f32_e64 v121, v51, v101 clamp
	v_add_f32_e64 v125, v55, v101 clamp
	v_add_f32_e64 v129, v59, v101 clamp
	v_add_f32_e64 v133, v63, v101 clamp
	v_add_f32_e64 v122, v52, v102 clamp
	v_add_f32_e64 v126, v56, v102 clamp
	v_add_f32_e64 v130, v60, v102 clamp
	v_add_f32_e64 v134, v64, v102 clamp
	v_add_f32_e64 v123, v53, v103 clamp
	v_add_f32_e64 v127, v57, v103 clamp
	v_add_f32_e64 v131, v61, v103 clamp
	v_add_f32_e64 v135, v65, v103 clamp
	v_fmac_f32_e32 v153, v78, v120
	v_fmac_f32_e32 v155, v78, v124
	v_fmac_f32_e32 v157, v78, v128
	v_fmac_f32_e32 v159, v78, v132
	v_fmac_f32_e32 v154, v79, v121
	v_fmac_f32_e32 v156, v79, v125
	v_fmac_f32_e32 v158, v79, v129
	v_fmac_f32_e32 v164, v79, v133
	v_fmac_f32_e32 v153, v80, v122
	v_fmac_f32_e32 v155, v80, v126
	v_fmac_f32_e32 v157, v80, v130
	v_fmac_f32_e32 v159, v80, v134
	v_fmac_f32_e32 v154, v81, v123
	v_fmac_f32_e32 v156, v81, v127
	v_fmac_f32_e32 v158, v81, v131
	v_fmac_f32_e32 v164, v81, v135
	v_add_f32_e32 v153, v153, v154
	v_add_f32_e32 v155, v155, v156
	v_add_f32_e32 v157, v157, v158
	v_add_f32_e32 v159, v159, v164
	ds_write2_b32 v1, v153, v155 offset1:32
	ds_write2_b32 v1, v157, v159 offset0:64 offset1:96
	v_add_u32_e32 v1, 0x1000, v1
	v_add_u32_e32 v152, s0, v86
	ds_read_b128 v[88:91], v152
	ds_read_b128 v[92:95], v152 offset:32
	ds_read_b128 v[96:99], v152 offset:64
	ds_read_b128 v[100:103], v152 offset:96
	s_addk_i32 s0, 0x200
	s_waitcnt lgkmcnt(4)
	v_add_f32_e64 v104, v2, v136 clamp
	v_add_f32_e64 v108, v6, v136 clamp
	v_add_f32_e64 v112, v10, v136 clamp
	v_add_f32_e64 v116, v14, v136 clamp
	v_add_f32_e64 v105, v3, v137 clamp
	v_add_f32_e64 v109, v7, v137 clamp
	v_add_f32_e64 v113, v11, v137 clamp
	v_add_f32_e64 v117, v15, v137 clamp
	v_add_f32_e64 v106, v4, v138 clamp
	v_add_f32_e64 v110, v8, v138 clamp
	v_add_f32_e64 v114, v12, v138 clamp
	v_add_f32_e64 v118, v16, v138 clamp
	v_add_f32_e64 v107, v5, v139 clamp
	v_add_f32_e64 v111, v9, v139 clamp
	v_add_f32_e64 v115, v13, v139 clamp
	v_add_f32_e64 v119, v17, v139 clamp
	v_mul_f32_e32 v153, v66, v104
	v_mul_f32_e32 v155, v66, v108
	v_mul_f32_e32 v157, v66, v112
	v_mul_f32_e32 v159, v66, v116
	v_mul_f32_e32 v154, v67, v105
	v_mul_f32_e32 v156, v67, v109
	v_mul_f32_e32 v158, v67, v113
	v_mul_f32_e32 v164, v67, v117
	v_fmac_f32_e32 v153, v68, v106
	v_fmac_f32_e32 v155, v68, v110
	v_fmac_f32_e32 v157, v68, v114
	v_fmac_f32_e32 v159, v68, v118
	v_fmac_f32_e32 v154, v69, v107
	v_fmac_f32_e32 v156, v69, v111
	v_fmac_f32_e32 v158, v69, v115
	v_fmac_f32_e32 v164, v69, v119
	v_add_f32_e64 v120, v18, v140 clamp
	v_add_f32_e64 v124, v22, v140 clamp
	v_add_f32_e64 v128, v26, v140 clamp
	v_add_f32_e64 v132, v30, v140 clamp
	v_add_f32_e64 v121, v19, v141 clamp
	v_add_f32_e64 v125, v23, v141 clamp
	v_add_f32_e64 v129, v27, v141 clamp
	v_add_f32_e64 v133, v31, v141 clamp
	v_add_f32_e64 v122, v20, v142 clamp
	v_add_f32_e64 v126, v24, v142 clamp
	v_add_f32_e64 v130, v28, v142 clamp
	v_add_f32_e64 v134, v32, v142 clamp
	v_add_f32_e64 v123, v21, v143 clamp
	v_add_f32_e64 v127, v25, v143 clamp
	v_add_f32_e64 v131, v29, v143 clamp
	v_add_f32_e64 v135, v33, v143 clamp
	v_fmac_f32_e32 v153, v70, v120
	v_fmac_f32_e32 v155, v70, v124
	v_fmac_f32_e32 v157, v70, v128
	v_fmac_f32_e32 v159, v70, v132
	v_fmac_f32_e32 v154, v71, v121
	v_fmac_f32_e32 v156, v71, v125
	v_fmac_f32_e32 v158, v71, v129
	v_fmac_f32_e32 v164, v71, v133
	v_fmac_f32_e32 v153, v72, v122
	v_fmac_f32_e32 v155, v72, v126
	v_fmac_f32_e32 v157, v72, v130
	v_fmac_f32_e32 v159, v72, v134
	v_fmac_f32_e32 v154, v73, v123
	v_fmac_f32_e32 v156, v73, v127
	v_fmac_f32_e32 v158, v73, v131
	v_fmac_f32_e32 v164, v73, v135
	v_add_f32_e64 v104, v34, v144 clamp
	v_add_f32_e64 v108, v38, v144 clamp
	v_add_f32_e64 v112, v42, v144 clamp
	v_add_f32_e64 v116, v46, v144 clamp
	v_add_f32_e64 v105, v35, v145 clamp
	v_add_f32_e64 v109, v39, v145 clamp
	v_add_f32_e64 v113, v43, v145 clamp
	v_add_f32_e64 v117, v47, v145 clamp
	v_add_f32_e64 v106, v36, v146 clamp
	v_add_f32_e64 v110, v40, v146 clamp
	v_add_f32_e64 v114, v44, v146 clamp
	v_add_f32_e64 v118, v48, v146 clamp
	v_add_f32_e64 v107, v37, v147 clamp
	v_add_f32_e64 v111, v41, v147 clamp
	v_add_f32_e64 v115, v45, v147 clamp
	v_add_f32_e64 v119, v49, v147 clamp
	v_fmac_f32_e32 v153, v74, v104
	v_fmac_f32_e32 v155, v74, v108
	v_fmac_f32_e32 v157, v74, v112
	v_fmac_f32_e32 v159, v74, v116
	v_fmac_f32_e32 v154, v75, v105
	v_fmac_f32_e32 v156, v75, v109
	v_fmac_f32_e32 v158, v75, v113
	v_fmac_f32_e32 v164, v75, v117
	v_fmac_f32_e32 v153, v76, v106
	v_fmac_f32_e32 v155, v76, v110
	v_fmac_f32_e32 v157, v76, v114
	v_fmac_f32_e32 v159, v76, v118
	v_fmac_f32_e32 v154, v77, v107
	v_fmac_f32_e32 v156, v77, v111
	v_fmac_f32_e32 v158, v77, v115
	v_fmac_f32_e32 v164, v77, v119
	v_add_f32_e64 v120, v50, v148 clamp
	v_add_f32_e64 v124, v54, v148 clamp
	v_add_f32_e64 v128, v58, v148 clamp
	v_add_f32_e64 v132, v62, v148 clamp
	v_add_f32_e64 v121, v51, v149 clamp
	v_add_f32_e64 v125, v55, v149 clamp
	v_add_f32_e64 v129, v59, v149 clamp
	v_add_f32_e64 v133, v63, v149 clamp
	v_add_f32_e64 v122, v52, v150 clamp
	v_add_f32_e64 v126, v56, v150 clamp
	v_add_f32_e64 v130, v60, v150 clamp
	v_add_f32_e64 v134, v64, v150 clamp
	v_add_f32_e64 v123, v53, v151 clamp
	v_add_f32_e64 v127, v57, v151 clamp
	v_add_f32_e64 v131, v61, v151 clamp
	v_add_f32_e64 v135, v65, v151 clamp
	v_fmac_f32_e32 v153, v78, v120
	v_fmac_f32_e32 v155, v78, v124
	v_fmac_f32_e32 v157, v78, v128
	v_fmac_f32_e32 v159, v78, v132
	v_fmac_f32_e32 v154, v79, v121
	v_fmac_f32_e32 v156, v79, v125
	v_fmac_f32_e32 v158, v79, v129
	v_fmac_f32_e32 v164, v79, v133
	v_fmac_f32_e32 v153, v80, v122
	v_fmac_f32_e32 v155, v80, v126
	v_fmac_f32_e32 v157, v80, v130
	v_fmac_f32_e32 v159, v80, v134
	v_fmac_f32_e32 v154, v81, v123
	v_fmac_f32_e32 v156, v81, v127
	v_fmac_f32_e32 v158, v81, v131
	v_fmac_f32_e32 v164, v81, v135
	v_add_f32_e32 v153, v153, v154
	v_add_f32_e32 v155, v155, v156
	v_add_f32_e32 v157, v157, v158
	v_add_f32_e32 v159, v159, v164
	ds_write2_b32 v1, v153, v155 offset1:32
	ds_write2_b32 v1, v157, v159 offset0:64 offset1:96
	v_add_u32_e32 v1, 0x1000, v1
	s_cmpk_eq_i32 s0, 0x1600
	s_cbranch_scc0 .Ltopic_loop
	v_lshl_or_b32 v1, v227, 12, v226
	s_waitcnt lgkmcnt(0)
	s_barrier
	ds_read2st64_b32 v[2:3], v1 offset0:40 offset1:42
	ds_read2st64_b32 v[4:5], v1 offset0:44 offset1:46
	ds_read2st64_b32 v[6:7], v1 offset0:48 offset1:50
	v_or_b32_e32 v13, 16, v227
	s_waitcnt lgkmcnt(2)
	v_add_f32_e32 v2, s18, v2
	v_add_f32_e32 v8, v2, v3
	ds_read2st64_b32 v[2:3], v1 offset0:52 offset1:54
	s_waitcnt lgkmcnt(2)
	v_add_f32_e32 v4, v8, v4
	v_add_f32_e32 v4, v4, v5
	s_waitcnt lgkmcnt(1)
	v_add_f32_e32 v4, v4, v6
	v_add_f32_e32 v4, v4, v7
	s_waitcnt lgkmcnt(0)
	v_add_f32_e32 v2, v4, v2
	v_add_f32_e32 v2, v2, v3
	v_mul_f32_e32 v2, 0xbfb8aa3b, v2
	v_exp_f32_e32 v2, v2
	s_nop 0
	v_add_f32_e32 v4, 1.0, v2
	v_div_scale_f32 v5, s[0:1], v4, v4, 1.0
	v_rcp_f32_e32 v6, v5
	v_div_scale_f32 v7, vcc, 1.0, v4, 1.0
	ds_read2st64_b32 v[2:3], v1 offset0:104 offset1:106
	v_fma_f32 v8, -v5, v6, 1.0
	v_fmac_f32_e32 v6, v8, v6
	v_mul_f32_e32 v8, v7, v6
	v_fma_f32 v9, -v5, v8, v7
	v_fmac_f32_e32 v8, v9, v6
	v_fma_f32 v5, -v5, v8, v7
	v_div_fmas_f32 v5, v5, v6, v8
	v_div_fixup_f32 v8, v5, v4, 1.0
	ds_read2st64_b32 v[4:5], v1 offset0:108 offset1:110
	ds_read2st64_b32 v[6:7], v1 offset0:112 offset1:114
	s_waitcnt lgkmcnt(2)
	v_add_f32_e32 v2, s18, v2
	v_add_f32_e32 v9, v2, v3
	ds_read2st64_b32 v[2:3], v1 offset0:116 offset1:118
	s_waitcnt lgkmcnt(2)
	v_add_f32_e32 v4, v9, v4
	v_add_f32_e32 v4, v4, v5
	s_waitcnt lgkmcnt(1)
	v_add_f32_e32 v4, v4, v6
	v_add_f32_e32 v4, v4, v7
	s_waitcnt lgkmcnt(0)
	v_add_f32_e32 v2, v4, v2
	v_add_f32_e32 v2, v2, v3
	v_mul_f32_e32 v2, 0xbfb8aa3b, v2
	v_exp_f32_e32 v2, v2
	v_lshlrev_b32_e32 v3, 2, v227
	v_or_b32_e32 v6, 8, v227
	v_mov_b32_e32 v7, 0x17000
	v_add_f32_e32 v10, 1.0, v2
	v_div_scale_f32 v5, s[0:1], v10, v10, 1.0
	v_rcp_f32_e32 v11, v5
	v_or_b32_e32 v4, 0x17000, v3
	v_lshl_or_b32 v12, v6, 2, v7
	v_or_b32_e32 v2, 0x17010, v3
	v_or_b32_e32 v3, 0x17030, v3
	v_lshl_or_b32 v7, v13, 2, v7
	ds_read_b32 v4, v4
	ds_read_b32 v14, v2
	ds_read_b32 v12, v12
	ds_read_b32 v15, v3
	ds_read_b32 v16, v7
	s_waitcnt lgkmcnt(4)
	v_fmaak_f32 v2, v8, v4, 0xbc23d70a
	v_max_f32_e32 v8, 0, v2
	v_fma_f32 v2, -v5, v11, 1.0
	v_fmac_f32_e32 v11, v2, v11
	v_div_scale_f32 v4, vcc, 1.0, v10, 1.0
	v_mul_f32_e32 v17, v4, v11
	v_lshl_or_b32 v18, v6, 12, v226
	ds_read2st64_b32 v[2:3], v18 offset0:40 offset1:42
	v_fma_f32 v6, -v5, v17, v4
	v_fmac_f32_e32 v17, v6, v11
	v_fma_f32 v19, -v5, v17, v4
	ds_read2st64_b32 v[4:5], v18 offset0:44 offset1:46
	ds_read2st64_b32 v[6:7], v18 offset0:48 offset1:50
	s_waitcnt lgkmcnt(2)
	v_add_f32_e32 v2, s18, v2
	v_add_f32_e32 v20, v2, v3
	ds_read2st64_b32 v[2:3], v18 offset0:52 offset1:54
	s_waitcnt lgkmcnt(2)
	v_add_f32_e32 v4, v20, v4
	v_add_f32_e32 v4, v4, v5
	s_waitcnt lgkmcnt(1)
	v_add_f32_e32 v4, v4, v6
	v_add_f32_e32 v4, v4, v7
	s_waitcnt lgkmcnt(0)
	v_add_f32_e32 v2, v4, v2
	v_add_f32_e32 v2, v2, v3
	v_mul_f32_e32 v2, 0xbfb8aa3b, v2
	v_exp_f32_e32 v2, v2
	v_div_fmas_f32 v3, v19, v11, v17
	v_div_fixup_f32 v3, v3, v10, 1.0
	v_mov_b32_e32 v9, 0xbc23d70a
	v_add_f32_e32 v10, 1.0, v2
	v_div_scale_f32 v4, s[0:1], v10, v10, 1.0
	v_rcp_f32_e32 v11, v4
	v_fmaak_f32 v2, v3, v14, 0xbc23d70a
	v_max_f32_e32 v2, 0, v2
	v_add_f32_e32 v8, v8, v2
	v_fma_f32 v2, -v4, v11, 1.0
	v_fmac_f32_e32 v11, v2, v11
	v_div_scale_f32 v5, vcc, 1.0, v10, 1.0
	v_mul_f32_e32 v14, v5, v11
	ds_read2st64_b32 v[2:3], v1 offset0:232 offset1:234
	v_fma_f32 v6, -v4, v14, v5
	v_fmac_f32_e32 v14, v6, v11
	v_fma_f32 v17, -v4, v14, v5
	ds_read2st64_b32 v[4:5], v1 offset0:236 offset1:238
	ds_read2st64_b32 v[6:7], v1 offset0:240 offset1:242
	s_waitcnt lgkmcnt(2)
	v_add_f32_e32 v2, s18, v2
	v_add_f32_e32 v18, v2, v3
	ds_read2st64_b32 v[2:3], v1 offset0:244 offset1:246
	s_waitcnt lgkmcnt(2)
	v_add_f32_e32 v1, v18, v4
	v_add_f32_e32 v1, v1, v5
	s_waitcnt lgkmcnt(1)
	v_add_f32_e32 v1, v1, v6
	v_add_f32_e32 v1, v1, v7
	s_waitcnt lgkmcnt(0)
	v_add_f32_e32 v1, v1, v2
	v_add_f32_e32 v1, v1, v3
	v_mul_f32_e32 v1, 0xbfb8aa3b, v1
	v_exp_f32_e32 v1, v1
	v_div_fmas_f32 v2, v17, v11, v14
	v_div_fixup_f32 v2, v2, v10, 1.0
	v_fmaak_f32 v2, v2, v12, 0xbc23d70a
	v_add_f32_e32 v1, 1.0, v1
	v_div_scale_f32 v4, s[0:1], v1, v1, 1.0
	v_rcp_f32_e32 v10, v4
	v_max_f32_e32 v2, 0, v2
	v_add_f32_e32 v8, v8, v2
	v_div_scale_f32 v5, vcc, 1.0, v1, 1.0
	v_fma_f32 v2, -v4, v10, 1.0
	v_fmac_f32_e32 v10, v2, v10
	v_mul_f32_e32 v11, v5, v10
	v_lshl_or_b32 v12, v13, 12, v226
	ds_read2st64_b32 v[2:3], v12 offset0:40 offset1:42
	v_fma_f32 v6, -v4, v11, v5
	v_fmac_f32_e32 v11, v6, v10
	v_fma_f32 v13, -v4, v11, v5
	ds_read2st64_b32 v[4:5], v12 offset0:44 offset1:46
	ds_read2st64_b32 v[6:7], v12 offset0:48 offset1:50
	s_waitcnt lgkmcnt(2)
	v_add_f32_e32 v2, s18, v2
	v_add_f32_e32 v14, v2, v3
	ds_read2st64_b32 v[2:3], v12 offset0:52 offset1:54
	s_waitcnt lgkmcnt(2)
	v_add_f32_e32 v4, v14, v4
	v_add_f32_e32 v4, v4, v5
	s_waitcnt lgkmcnt(1)
	v_add_f32_e32 v4, v4, v6
	v_add_f32_e32 v4, v4, v7
	s_waitcnt lgkmcnt(0)
	v_add_f32_e32 v2, v4, v2
	v_add_f32_e32 v2, v2, v3
	v_mul_f32_e32 v2, 0xbfb8aa3b, v2
	v_exp_f32_e32 v2, v2
	v_div_fmas_f32 v3, v13, v10, v11
	v_div_fixup_f32 v1, v3, v1, 1.0
	v_fmaak_f32 v1, v1, v15, 0xbc23d70a
	v_add_f32_e32 v2, 1.0, v2
	v_div_scale_f32 v3, s[0:1], v2, v2, 1.0
	v_rcp_f32_e32 v4, v3
	v_max_f32_e32 v1, 0, v1
	v_add_f32_e32 v1, v8, v1
	s_lshl_b32 s0, s42, 5
	v_fma_f32 v5, -v3, v4, 1.0
	v_fmac_f32_e32 v4, v5, v4
	v_div_scale_f32 v5, vcc, 1.0, v2, 1.0
	v_mul_f32_e32 v6, v5, v4
	v_fma_f32 v7, -v3, v6, v5
	v_fmac_f32_e32 v6, v7, v4
	v_fma_f32 v3, -v3, v6, v5
	v_div_fmas_f32 v3, v3, v4, v6
	v_div_fixup_f32 v2, v3, v2, 1.0
	v_fmac_f32_e32 v9, v2, v16
	v_max_f32_e32 v2, 0, v9
	v_add_f32_e32 v2, v1, v2
	v_mov_b32_e32 v1, 0x16800
	v_lshl_or_b32 v1, v0, 2, v1
	v_cmp_gt_u32_e32 vcc, s0, v0
	ds_write_b32 v1, v2
	s_waitcnt lgkmcnt(0)
	s_barrier
	s_and_saveexec_b64 s[0:1], vcc
	s_cbranch_execz .LBB1_57
	ds_read2st64_b32 v[2:3], v1 offset1:2
	ds_read2st64_b32 v[4:5], v1 offset0:4 offset1:6
	v_add_u32_e32 v0, s33, v0
	v_ashrrev_i32_e32 v1, 31, v0
	v_lshl_add_u64 v[6:7], v[0:1], 2, s[10:11]
	s_waitcnt lgkmcnt(1)
	v_add_f32_e32 v1, v2, v3
	s_waitcnt lgkmcnt(0)
	v_add_f32_e32 v1, v1, v4
	v_add_f32_e32 v1, v1, v5
	v_add_u32_e32 v0, 0x7d00, v0
	v_mul_f32_e32 v2, 0x3d4ccccd, v1
	v_ashrrev_i32_e32 v1, 31, v0
	v_lshl_add_u64 v[0:1], v[0:1], 2, s[10:11]
	global_store_dword v[6:7], v2, off
	global_store_dword v[0:1], v2, off
